# h table L2 prefetch after count barrier; h1s stores write-through
# baseline (speedup 1.0000x reference)
.LBB2_2:
	s_or_b64 exec, exec, s[4:5]
	s_load_dwordx8 s[48:55], s[0:1], 0x30
	s_load_dwordx2 s[46:47], s[0:1], 0x0
	s_load_dwordx8 s[56:63], s[0:1], 0x10
	s_and_b32 s3, s2, 7
	s_mul_i32 s4, s3, 31
	s_min_u32 s3, s3, 2
	s_ashr_i32 s2, s2, 3
	s_mov_b32 s83, s2
	v_and_b32_e32 v45, 63, v0
	s_add_i32 s64, s3, s2
	v_lshrrev_b32_e32 v6, 6, v0
	s_add_i32 s64, s64, s4
	v_cmp_gt_u32_e64 s[4:5], 16, v45
	v_mov_b32_e32 v4, 0
	v_mov_b32_e32 v2, 0
	v_mov_b32_e32 v3, 0
	s_load_dwordx2 s[6:7], s[0:1], 0x8
	v_lshlrev_b32_e32 v50, 2, v0
	s_movk_i32 s2, 0x280
	v_cmp_gt_u32_e32 vcc, s2, v0
	s_waitcnt lgkmcnt(0)
	s_and_saveexec_b64 s[2:3], vcc
	s_cbranch_execz .Lpro_a
	global_load_dword v100, v50, s[48:49]

.LBB2_99:
	s_movk_i32 s2, 0x190
	v_mov_b32_e32 v2, 0x10000
	v_cmp_gt_u32_e32 vcc, s2, v0
	v_lshl_or_b32 v35, v0, 2, v2
	v_mov_b32_e32 v36, 0
	v_mov_b32_e32 v37, 0
	s_waitcnt lgkmcnt(0)
	s_barrier
	s_lshl_b32 s84, s83, 10
	v_add_u32_e32 v112, s84, v0
	v_min_u32_e32 v112, 0x61a7, v112
	v_lshlrev_b32_e32 v112, 7, v112
	global_load_dword v112, v112, s[56:57]
	s_and_saveexec_b64 s[2:3], vcc
	ds_read_b32 v37, v35
	s_or_b64 exec, exec, s[2:3]
	s_and_saveexec_b64 s[2:3], vcc
	ds_read_b32 v36, v35 offset:1600
	s_or_b64 exec, exec, s[2:3]
	v_mov_b32_e32 v38, 0
	v_mov_b32_e32 v39, 0
	s_and_saveexec_b64 s[2:3], vcc
	ds_read_b32 v39, v35 offset:3200
	s_or_b64 exec, exec, s[2:3]
	s_and_saveexec_b64 s[2:3], vcc
	ds_read_b32 v38, v35 offset:4800
	s_or_b64 exec, exec, s[2:3]
	v_mov_b32_e32 v40, 0
	v_mov_b32_e32 v41, 0
	s_and_saveexec_b64 s[2:3], vcc
	ds_read_b32 v41, v35 offset:6400
	s_or_b64 exec, exec, s[2:3]
	s_and_saveexec_b64 s[2:3], vcc
	ds_read_b32 v40, v35 offset:8000
	s_or_b64 exec, exec, s[2:3]
	v_mov_b32_e32 v43, 0
	v_mov_b32_e32 v44, 0
	s_and_saveexec_b64 s[2:3], vcc
	ds_read_b32 v44, v35 offset:9600
	s_or_b64 exec, exec, s[2:3]
	s_and_saveexec_b64 s[2:3], vcc
	ds_read_b32 v43, v35 offset:11200
	s_or_b64 exec, exec, s[2:3]
	v_mov_b32_e32 v46, 0
	v_mov_b32_e32 v47, 0
	s_and_saveexec_b64 s[2:3], vcc
	ds_read_b32 v47, v35 offset:12800
	s_or_b64 exec, exec, s[2:3]
	s_and_saveexec_b64 s[2:3], vcc
	ds_read_b32 v46, v35 offset:14400
	s_or_b64 exec, exec, s[2:3]
	v_mov_b32_e32 v53, 0
	v_mov_b32_e32 v54, 0
	s_and_saveexec_b64 s[2:3], vcc
	ds_read_b32 v54, v35 offset:16000
	s_or_b64 exec, exec, s[2:3]
	s_and_saveexec_b64 s[2:3], vcc
	ds_read_b32 v53, v35 offset:17600
	s_or_b64 exec, exec, s[2:3]
	v_mov_b32_e32 v55, 0
	v_mov_b32_e32 v56, 0
	s_and_saveexec_b64 s[2:3], vcc
	ds_read_b32 v56, v35 offset:19200
	s_or_b64 exec, exec, s[2:3]
	s_and_saveexec_b64 s[2:3], vcc
	ds_read_b32 v55, v35 offset:20800
	s_or_b64 exec, exec, s[2:3]
	v_mov_b32_e32 v2, 0
	v_mov_b32_e32 v57, 0
	s_and_saveexec_b64 s[2:3], vcc
	ds_read_b32 v57, v35 offset:22400
	s_or_b64 exec, exec, s[2:3]
	s_and_saveexec_b64 s[2:3], vcc
	ds_read_b32 v2, v35 offset:24000
	s_or_b64 exec, exec, s[2:3]
	s_waitcnt lgkmcnt(0)
	v_add_u32_e32 v3, v36, v37
	v_add3_u32 v3, v39, v3, v38
	v_add3_u32 v3, v41, v3, v40
	v_add3_u32 v3, v44, v3, v43
	v_add3_u32 v3, v47, v3, v46
	v_add3_u32 v3, v54, v3, v53
	v_add3_u32 v3, v56, v3, v55
	v_add3_u32 v58, v57, v3, v2
	v_mbcnt_lo_u32_b32 v2, -1, 0
	v_mbcnt_hi_u32_b32 v51, -1, v2
	v_and_b32_e32 v52, 64, v51
	v_add_u32_e32 v2, -1, v51
	v_cmp_lt_i32_e64 s[2:3], v2, v52
	v_add_u32_e32 v3, -2, v51
	s_nop 0
	v_cndmask_b32_e64 v2, v2, v51, s[2:3]
	v_lshlrev_b32_e32 v2, 2, v2
	ds_bpermute_b32 v2, v2, v58
	v_cmp_ne_u32_e64 s[2:3], 0, v45
	s_waitcnt lgkmcnt(0)
	s_nop 0
	v_cndmask_b32_e64 v2, 0, v2, s[2:3]
	v_cmp_lt_i32_e64 s[2:3], v3, v52
	v_add_u32_e32 v2, v2, v58
	s_nop 0
	v_cndmask_b32_e64 v3, v3, v51, s[2:3]
	v_lshlrev_b32_e32 v3, 2, v3
	ds_bpermute_b32 v3, v3, v2
	v_cmp_lt_u32_e64 s[2:3], 1, v45
	s_waitcnt lgkmcnt(0)
	s_nop 0
	v_cndmask_b32_e64 v3, 0, v3, s[2:3]
	v_add_u32_e32 v2, v3, v2
	v_add_u32_e32 v3, -4, v51
	v_cmp_lt_i32_e64 s[2:3], v3, v52
	s_nop 1
	v_cndmask_b32_e64 v3, v3, v51, s[2:3]
	v_lshlrev_b32_e32 v3, 2, v3
	ds_bpermute_b32 v3, v3, v2
	v_cmp_lt_u32_e64 s[2:3], 3, v45
	s_waitcnt lgkmcnt(0)
	s_nop 0
	v_cndmask_b32_e64 v3, 0, v3, s[2:3]
	v_add_u32_e32 v2, v3, v2
	v_add_u32_e32 v3, -8, v51
	v_cmp_lt_i32_e64 s[2:3], v3, v52
	s_nop 1
	v_cndmask_b32_e64 v3, v3, v51, s[2:3]
	v_lshlrev_b32_e32 v3, 2, v3
	ds_bpermute_b32 v3, v3, v2
	v_cmp_lt_u32_e64 s[2:3], 7, v45
	s_waitcnt lgkmcnt(0)
	s_nop 0
	v_cndmask_b32_e64 v3, 0, v3, s[2:3]
	v_add_u32_e32 v2, v3, v2
	v_add_u32_e32 v3, -16, v51
	v_cmp_lt_i32_e64 s[2:3], v3, v52
	s_nop 1
	v_cndmask_b32_e64 v3, v3, v51, s[2:3]
	v_lshlrev_b32_e32 v3, 2, v3
	ds_bpermute_b32 v3, v3, v2
	s_waitcnt lgkmcnt(0)
	v_cndmask_b32_e64 v3, v3, 0, s[4:5]
	v_add_u32_e32 v2, v3, v2
	v_subrev_u32_e32 v3, 32, v51
	v_cmp_lt_i32_e64 s[2:3], v3, v52
	s_nop 1
	v_cndmask_b32_e64 v3, v3, v51, s[2:3]
	v_lshlrev_b32_e32 v3, 2, v3
	ds_bpermute_b32 v3, v3, v2
	v_cmp_lt_u32_e64 s[2:3], 31, v45
	s_waitcnt lgkmcnt(0)
	s_nop 0
	v_cndmask_b32_e64 v3, 0, v3, s[2:3]
	v_add_u32_e32 v59, v3, v2
	v_cmp_eq_u32_e64 s[2:3], 63, v45
	s_and_saveexec_b64 s[4:5], s[2:3]
	s_xor_b64 s[2:3], exec, s[4:5]
	v_mov_b32_e32 v2, 0x17cf0
	v_lshl_add_u32 v2, v6, 2, v2
	ds_write_b32 v2, v59
	s_or_b64 exec, exec, s[2:3]
	v_mov_b32_e32 v2, 0x17cf0
	v_mov_b32_e32 v3, 0x17d00
	s_waitcnt lgkmcnt(0)
	s_barrier
	ds_read_b128 v[14:17], v2
	ds_read_b128 v[6:9], v3
	v_mov_b32_e32 v2, 0x17d10
	v_mov_b32_e32 v3, 0x17d20
	ds_read_b128 v[10:13], v2
	ds_read_b128 v[2:5], v3
	s_and_saveexec_b64 s[2:3], vcc
	s_cbranch_execz .LBB2_135
	v_cmp_lt_u32_e32 vcc, 63, v0
	s_movk_i32 s4, 0x7f
	v_sub_u32_e32 v58, v59, v58
	s_waitcnt lgkmcnt(3)
	v_cndmask_b32_e32 v60, 0, v14, vcc
	v_cmp_lt_u32_e32 vcc, s4, v0
	s_movk_i32 s4, 0xbf
	s_nop 0
	v_cndmask_b32_e32 v59, 0, v15, vcc
	v_cmp_lt_u32_e32 vcc, s4, v0
	s_movk_i32 s4, 0xff
	v_add3_u32 v58, v60, v58, v59
	v_cndmask_b32_e32 v59, 0, v16, vcc
	v_cmp_lt_u32_e32 vcc, s4, v0
	s_movk_i32 s4, 0x13f
	s_nop 0
	v_cndmask_b32_e32 v60, 0, v17, vcc
	v_cmp_lt_u32_e32 vcc, s4, v0
	s_movk_i32 s4, 0x17f
	v_add3_u32 v58, v58, v59, v60
	s_waitcnt lgkmcnt(2)
	v_cndmask_b32_e32 v59, 0, v6, vcc
	v_cmp_lt_u32_e32 vcc, s4, v0
	s_nop 1
	v_cndmask_b32_e32 v60, 0, v7, vcc
	v_add3_u32 v58, v58, v59, v60
	v_add_u32_e32 v37, v37, v58
	v_add_u32_e32 v36, v36, v37
	ds_write_b32 v35, v36 offset:3200
	v_add_u32_e32 v36, v39, v36
	ds_write_b32 v35, v36 offset:4800
	v_add_u32_e32 v36, v38, v36
	ds_write_b32 v35, v36 offset:6400
	v_add_u32_e32 v36, v41, v36
	ds_write_b32 v35, v36 offset:8000
	v_add_u32_e32 v36, v40, v36
	ds_write_b32 v35, v36 offset:9600
	v_add_u32_e32 v36, v44, v36
	ds_write_b32 v35, v36 offset:11200
	v_add_u32_e32 v36, v43, v36
	ds_write_b32 v35, v36 offset:12800
	v_add_u32_e32 v36, v47, v36
	ds_write_b32 v35, v36 offset:14400
	v_add_u32_e32 v36, v46, v36
	ds_write_b32 v35, v36 offset:16000
	v_add_u32_e32 v36, v54, v36
	ds_write_b32 v35, v36 offset:17600
	v_add_u32_e32 v36, v53, v36
	ds_write_b32 v35, v36 offset:19200
	v_add_u32_e32 v36, v56, v36
	ds_write_b32 v35, v36 offset:20800
	v_add_u32_e32 v36, v55, v36
	ds_write_b32 v35, v36 offset:22400
	v_add_u32_e32 v36, v57, v36
	ds_write_b32 v35, v58
	ds_write_b32 v35, v37 offset:1600
	ds_write_b32 v35, v36 offset:24000
	v_mov_b32_e32 v35, 0x16e00
	v_lshl_add_u32 v35, v0, 2, v35
	ds_write_b32 v35, v58

.LBB2_284:
	v_lshlrev_b64 v[22:23], 5, v[64:65]
	v_lshlrev_b32_e32 v20, 4, v44
	v_mov_b32_e32 v21, 0
	v_lshl_add_u64 v[22:23], s[62:63], 0, v[22:23]
	s_waitcnt vmcnt(0) lgkmcnt(0)
	v_fma_f32 v6, v53, v6, v100
	v_fma_f32 v7, v53, v7, v101
	v_fma_f32 v8, v53, v8, v102
	v_fma_f32 v13, v53, v9, v103
	v_fma_f32 v9, v53, v2, v104
	v_fma_f32 v10, v53, v3, v105
	v_fma_f32 v11, v53, v4, v106
	v_fma_f32 v17, v53, v5, v107
	v_max_f32_e32 v2, 0, v6
	v_max_f32_e32 v3, 0, v7
	v_max_f32_e32 v4, 0, v8
	v_max_f32_e32 v5, 0, v13
	v_max_f32_e32 v6, 0, v9
	v_max_f32_e32 v7, 0, v10
	v_max_f32_e32 v8, 0, v11
	v_max_f32_e32 v9, 0, v17
	v_pk_mul_f32 v[2:3], v[108:109], v[2:3] op_sel_hi:[0,1]
	v_pk_mul_f32 v[4:5], v[108:109], v[4:5] op_sel_hi:[0,1]
	v_pk_mul_f32 v[6:7], v[108:109], v[6:7] op_sel_hi:[0,1]
	v_pk_mul_f32 v[8:9], v[108:109], v[8:9] op_sel_hi:[0,1]
	v_cvt_pk_bf16_f32 v2, v2, v3
	v_cvt_pk_bf16_f32 v3, v4, v5
	v_cvt_pk_bf16_f32 v4, v6, v7
	v_cvt_pk_bf16_f32 v5, v8, v9
	v_lshl_add_u64 v[6:7], v[22:23], 0, v[20:21]
	global_store_dwordx4 v[6:7], v[2:5], off sc0 sc1
